# same as v22 with one more wait state (s_nop 8) before first S2 read in both loop-2 copies (hazard distance 12)
# baseline (speedup 1.0000x reference)
.Ll2f_top:
	v_exp_f32_e32 v215, v66
	s_nop 8
	v_exp_f32_e32 v216, v82
	v_exp_f32_e32 v217, v67
	v_exp_f32_e32 v214, v83
	v_exp_f32_e32 v219, v68
	v_exp_f32_e32 v220, v84
	ds_read_b128 v[98:101], v186 offset:18432
	ds_read_b128 v[162:165], v186 offset:18464
	ds_read_b128 v[194:197], v186 offset:27648
	ds_read_b128 v[198:201], v186 offset:27680
	ds_read_b128 v[202:205], v186 offset:18496
	ds_read_b128 v[206:209], v186 offset:18528
	ds_read_b128 v[210:213], v186 offset:27712
	ds_read_b128 v[166:169], v186 offset:27744
	v_exp_f32_e32 v221, v69
	v_exp_f32_e32 v218, v85
	s_waitcnt lgkmcnt(7)
	v_mfma_f32_32x32x16_f16 v[98:113], v[98:101], v[114:117], v[240:255]
	v_exp_f32_e32 v223, v70
	v_exp_f32_e32 v70, v86
	v_exp_f32_e32 v71, v71
	v_exp_f32_e32 v222, v87
	v_exp_f32_e32 v225, v72
	v_exp_f32_e32 v226, v88
	v_exp_f32_e32 v227, v73
	v_exp_f32_e32 v224, v89
	s_waitcnt lgkmcnt(6)
	v_mfma_f32_32x32x16_f16 v[98:113], v[162:165], v[118:121], v[98:113]
	v_exp_f32_e32 v229, v74
	v_exp_f32_e32 v230, v90
	v_exp_f32_e32 v231, v75
	v_exp_f32_e32 v228, v91
	v_exp_f32_e32 v233, v76
	v_exp_f32_e32 v234, v92
	v_exp_f32_e32 v235, v77
	v_exp_f32_e32 v232, v93
	s_waitcnt lgkmcnt(3)
	v_mfma_f32_32x32x16_f16 v[98:113], v[202:205], v[122:125], v[98:113]
	v_exp_f32_e32 v237, v78
	v_exp_f32_e32 v162, v94
	v_exp_f32_e32 v163, v79
	v_exp_f32_e32 v236, v95
	v_exp_f32_e32 v165, v80
	v_exp_f32_e32 v202, v96
	v_exp_f32_e32 v203, v81
	v_exp_f32_e32 v193, v97
	s_waitcnt lgkmcnt(2)
	v_mfma_f32_32x32x16_f16 v[98:113], v[206:209], v[126:129], v[98:113]
	s_waitcnt vmcnt(3)
	ds_write_b128 v185, v[146:149]
	s_waitcnt vmcnt(2)
	ds_write_b128 v185, v[150:153] offset:9216
	s_waitcnt vmcnt(1)
	ds_write_b128 v185, v[154:157] offset:55296
	s_waitcnt vmcnt(0)
	ds_write_b128 v185, v[158:161] offset:64512
	v_fma_f32 v150, v176, v216, v215
	v_fma_f32 v151, v176, v214, v217
	ds_read_b128 v[66:69], v189
	ds_read_b128 v[88:91], v189 offset:1152
	v_fma_f32 v152, v176, v220, v219
	v_fma_f32 v153, v176, v218, v221
	ds_read_b128 v[92:95], v189 offset:2304
	ds_read_b128 v[146:149], v189 offset:3456
	v_fma_f32 v154, v176, v70, v223
	v_fma_f32 v155, v176, v222, v71
	ds_write_b128 v190, v[150:153]
	v_fma_f32 v156, v176, v226, v225
	v_fma_f32 v157, v176, v224, v227
	ds_write_b128 v190, v[154:157] offset:16
	v_fma_f32 v158, v176, v230, v229
	v_fma_f32 v159, v176, v228, v231
	v_cvt_pk_f16_f32 v157, v156, v157
	v_fma_f32 v160, v176, v234, v233
	v_fma_f32 v161, v176, v232, v235
	ds_write_b128 v190, v[158:161] offset:64
	v_fma_f32 v162, v176, v162, v237
	v_fma_f32 v163, v176, v236, v163
	v_cvt_pk_f16_f32 v156, v154, v155
	v_fma_f32 v164, v176, v202, v165
	v_fma_f32 v165, v176, v193, v203
	ds_write_b128 v190, v[162:165] offset:80
	v_cvt_pk_f16_f32 v155, v152, v153
	v_cvt_pk_f16_f32 v154, v150, v151
	ds_read_b128 v[150:153], v191 offset:36864
	s_cmp_eq_u32 s19, 0
	s_cselect_b64 vcc, -1, 0
	s_add_i32 s20, s16, s1
	v_mfma_f32_32x32x16_f16 v[72:87], v[194:197], v[130:133], 0
	ds_read_b128 v[194:197], v191 offset:36896
	s_add_i32 s2, s20, 0x7c0
	s_and_b32 s2, s2, 0x7c0
	s_lshl_b32 s2, s2, 2
	v_lshl_add_u64 v[70:71], v[174:175], 0, s[2:3]
	v_cndmask_b32_e32 v71, v71, v179, vcc
	v_cndmask_b32_e32 v70, v70, v178, vcc
	s_waitcnt lgkmcnt(1)
	v_mfma_f32_32x32x16_f16 v[50:65], v[154:157], v[150:153], v[50:65]
	ds_read_b128 v[150:153], v191 offset:41472
	global_store_dwordx4 v[70:71], v[66:69], off nt
	ds_read_b128 v[66:69], v191 offset:41504
	v_cvt_pk_f16_f32 v165, v164, v165
	v_cvt_pk_f16_f32 v164, v162, v163
	v_cvt_pk_f16_f32 v163, v160, v161
	v_cvt_pk_f16_f32 v162, v158, v159
	s_waitcnt lgkmcnt(1)
	v_mfma_f32_32x32x16_f16 v[34:49], v[154:157], v[150:153], v[34:49]
	v_add_co_u32_e32 v96, vcc, s5, v70
	s_min_u32 s2, s19, 28
	s_nop 0
	v_addc_co_u32_e32 v97, vcc, 0, v71, vcc
	global_store_dwordx4 v[96:97], v[88:91], off nt
	s_add_i32 s21, s17, s2
	s_waitcnt lgkmcnt(0)
	v_mfma_f32_32x32x16_f16 v[34:49], v[162:165], v[66:69], v[34:49]
	ds_read_b128 v[66:69], v191 offset:46080
	v_add_co_u32_e32 v88, vcc, s13, v70
	s_lshl_b32 s2, s21, 13
	s_nop 0
	v_addc_co_u32_e32 v89, vcc, 0, v71, vcc
	global_store_dwordx4 v[88:89], v[92:95], off nt
	ds_read_b128 v[88:91], v191 offset:46112
	s_waitcnt lgkmcnt(1)
	v_mfma_f32_32x32x16_f16 v[18:33], v[154:157], v[66:69], v[18:33]
	v_add_co_u32_e32 v70, vcc, s14, v70
	s_and_b32 s2, s2, 0x3e000
	s_nop 0
	v_addc_co_u32_e32 v71, vcc, 0, v71, vcc
	v_lshl_add_u64 v[66:67], v[170:171], 0, s[2:3]
	v_add_co_u32_e32 v68, vcc, s15, v66
	global_store_dwordx4 v[70:71], v[146:149], off nt
	s_nop 0
	v_addc_co_u32_e32 v69, vcc, 0, v67, vcc
	s_waitcnt lgkmcnt(0)
	v_mfma_f32_32x32x16_f16 v[18:33], v[162:165], v[88:91], v[18:33]
	global_load_dwordx4 v[88:91], v[66:67], off
	global_load_dwordx4 v[92:95], v[68:69], off
	ds_read_b128 v[66:69], v191 offset:50688
	ds_read_b128 v[146:149], v191 offset:50720
	s_min_u32 s2, s19, 29
	s_add_i32 s2, s0, s2
	s_lshl_b32 s2, s2, 7
	s_and_b32 s2, s2, 0xf80
	s_waitcnt lgkmcnt(1)
	v_mfma_f32_32x32x16_f16 v[2:17], v[154:157], v[66:69], v[2:17]
	v_lshl_add_u64 v[66:67], v[172:173], 0, s[2:3]
	v_add_co_u32_e32 v68, vcc, s10, v66
	s_nop 0
	v_addc_co_u32_e32 v69, vcc, 0, v67, vcc
	global_load_dwordx4 v[150:153], v[66:67], off
	global_load_dwordx4 v[154:157], v[68:69], off
	v_mfma_f32_32x32x16_f16 v[72:87], v[198:201], v[134:137], v[72:87]
	v_exp_f32_e32 v97, v98
	s_waitcnt lgkmcnt(0)
	s_barrier
	v_mfma_f32_32x32x16_f16 v[72:87], v[210:213], v[138:141], v[72:87]
	v_mfma_f32_32x32x16_f16 v[72:87], v[166:169], v[142:145], v[72:87]
	v_mfma_f32_32x32x16_f16 v[50:65], v[162:165], v[194:197], v[50:65]
	s_nop 10
	v_exp_f32_e32 v166, v72
	v_exp_f32_e32 v167, v99
	v_exp_f32_e32 v96, v73
	v_exp_f32_e32 v99, v100
	v_exp_f32_e32 v168, v74
	v_exp_f32_e32 v169, v101
	v_exp_f32_e32 v98, v75
	v_exp_f32_e32 v101, v102
	v_exp_f32_e32 v210, v76
	v_exp_f32_e32 v211, v103
	v_exp_f32_e32 v100, v77
	v_exp_f32_e32 v103, v104
	v_exp_f32_e32 v212, v78
	v_exp_f32_e32 v213, v105
	v_exp_f32_e32 v102, v79
	v_exp_f32_e32 v105, v106
	v_exp_f32_e32 v214, v80
	v_exp_f32_e32 v215, v107
	v_mfma_f32_32x32x16_f16 v[2:17], v[162:165], v[146:149], v[2:17]
	ds_read_b128 v[66:69], v186
	ds_read_b128 v[158:161], v186 offset:32
	ds_read_b128 v[194:197], v186 offset:9216
	ds_read_b128 v[198:201], v186 offset:9248
	ds_read_b128 v[202:205], v186 offset:64
	ds_read_b128 v[206:209], v186 offset:96
	ds_read_b128 v[146:149], v186 offset:9280
	ds_read_b128 v[162:165], v186 offset:9312
	v_exp_f32_e32 v104, v81
	v_exp_f32_e32 v107, v108
	v_exp_f32_e32 v216, v82
	s_waitcnt lgkmcnt(7)
	v_mfma_f32_32x32x16_f16 v[66:81], v[66:69], v[114:117], v[240:255]
	v_exp_f32_e32 v217, v109
	v_exp_f32_e32 v106, v83
	v_exp_f32_e32 v109, v110
	v_exp_f32_e32 v218, v84
	s_waitcnt lgkmcnt(6)
	v_mfma_f32_32x32x16_f16 v[66:81], v[158:161], v[118:121], v[66:81]
	v_exp_f32_e32 v219, v111
	v_exp_f32_e32 v108, v85
	v_exp_f32_e32 v111, v112
	s_waitcnt lgkmcnt(3)
	v_mfma_f32_32x32x16_f16 v[66:81], v[202:205], v[122:125], v[66:81]
	v_exp_f32_e32 v202, v86
	v_exp_f32_e32 v203, v113
	v_exp_f32_e32 v110, v87
	s_waitcnt lgkmcnt(2)
	v_mfma_f32_32x32x16_f16 v[66:81], v[206:209], v[126:129], v[66:81]
	s_waitcnt vmcnt(3)
	ds_write_b128 v185, v[88:91] offset:18432
	s_waitcnt vmcnt(2)
	ds_write_b128 v185, v[92:95] offset:27648
	s_waitcnt vmcnt(1)
	ds_write_b128 v185, v[150:153] offset:36864
	s_waitcnt vmcnt(0)
	ds_write_b128 v185, v[154:157] offset:46080
	v_fma_f32 v150, v176, v166, v97
	v_fma_f32 v151, v176, v96, v167
	v_mfma_f32_32x32x16_f16 v[82:97], v[194:197], v[130:133], 0
	v_fma_f32 v152, v176, v168, v99
	v_fma_f32 v153, v176, v98, v169
	v_fma_f32 v154, v176, v210, v101
	v_fma_f32 v155, v176, v100, v211
	v_fma_f32 v156, v176, v212, v103
	v_fma_f32 v157, v176, v102, v213
	v_fma_f32 v158, v176, v214, v105
	v_fma_f32 v159, v176, v104, v215
	v_fma_f32 v160, v176, v216, v107
	v_fma_f32 v161, v176, v106, v217
	v_fma_f32 v166, v176, v218, v109
	v_fma_f32 v167, v176, v108, v219
	v_fma_f32 v168, v176, v202, v111
	v_fma_f32 v169, v176, v110, v203
	ds_read_b128 v[98:101], v189
	ds_read_b128 v[102:105], v189 offset:1152
	ds_read_b128 v[106:109], v189 offset:2304
	ds_read_b128 v[110:113], v189 offset:3456
	ds_write_b128 v190, v[150:153]
	ds_write_b128 v190, v[154:157] offset:16
	ds_write_b128 v190, v[158:161] offset:64
	ds_write_b128 v190, v[166:169] offset:80
	v_cvt_pk_f16_f32 v157, v156, v157
	v_cvt_pk_f16_f32 v156, v154, v155
	v_cvt_pk_f16_f32 v155, v152, v153
	v_cvt_pk_f16_f32 v154, v150, v151
	ds_read_b128 v[150:153], v191 offset:55296
	ds_read_b128 v[194:197], v191 offset:55328
	v_mfma_f32_32x32x16_f16 v[82:97], v[198:201], v[134:137], v[82:97]
	s_and_b32 s2, s20, 0x7c0
	s_min_u32 s20, s19, 27
	s_lshl_b32 s2, s2, 2
	s_add_i32 s20, s18, s20
	v_lshl_add_u64 v[210:211], v[174:175], 0, s[2:3]
	s_lshl_b32 s2, s20, 13
	s_and_b32 s2, s2, 0x3e000
	s_waitcnt lgkmcnt(1)
	v_mfma_f32_32x32x16_f16 v[50:65], v[154:157], v[150:153], v[50:65]
	ds_read_b128 v[150:153], v191 offset:59904
	ds_read_b128 v[198:201], v191 offset:59936
	s_lshl_b32 s21, s21, 7
	v_cvt_pk_f16_f32 v169, v168, v169
	v_cvt_pk_f16_f32 v168, v166, v167
	v_cvt_pk_f16_f32 v166, v158, v159
	v_cvt_pk_f16_f32 v167, v160, v161
	s_addk_i32 s1, 0x80
	s_waitcnt lgkmcnt(1)
	v_mfma_f32_32x32x16_f16 v[34:49], v[154:157], v[150:153], v[34:49]
	ds_read_b128 v[150:153], v191 offset:64512
	ds_read_b128 v[202:205], v191 offset:64544
	s_waitcnt lgkmcnt(1)
	v_mfma_f32_32x32x16_f16 v[18:33], v[154:157], v[150:153], v[18:33]
	ds_read_b128 v[150:153], v192 offset:13824
	ds_read_b128 v[206:209], v192 offset:13856
	v_mfma_f32_32x32x16_f16 v[82:97], v[146:149], v[138:141], v[82:97]
	v_lshl_add_u64 v[146:147], v[170:171], 0, s[2:3]
	s_and_b32 s2, s21, 0xf80
	v_lshl_add_u64 v[158:159], v[172:173], 0, s[2:3]
	s_add_i32 s2, s19, 2
	s_cmp_lt_u32 s19, 30
	s_mov_b32 s19, s2
	s_waitcnt lgkmcnt(1)
	v_mfma_f32_32x32x16_f16 v[2:17], v[154:157], v[150:153], v[2:17]
	v_add_co_u32_e32 v150, vcc, s15, v146
	s_nop 1
	v_addc_co_u32_e32 v151, vcc, 0, v147, vcc
	global_load_dwordx4 v[146:149], v[146:147], off
	s_nop 0
	global_load_dwordx4 v[150:153], v[150:151], off
	s_nop 0
	global_load_dwordx4 v[154:157], v[158:159], off
	v_add_co_u32_e32 v158, vcc, s10, v158
	v_mfma_f32_32x32x16_f16 v[50:65], v[166:169], v[194:197], v[50:65]
	s_nop 0
	v_addc_co_u32_e32 v159, vcc, 0, v159, vcc
	global_load_dwordx4 v[158:161], v[158:159], off
	v_add_co_u32_e32 v194, vcc, s5, v210
	s_nop 1
	v_addc_co_u32_e32 v195, vcc, 0, v211, vcc
	v_mfma_f32_32x32x16_f16 v[34:49], v[166:169], v[198:201], v[34:49]
	v_add_co_u32_e32 v196, vcc, s13, v210
	s_nop 1
	v_addc_co_u32_e32 v197, vcc, 0, v211, vcc
	v_mfma_f32_32x32x16_f16 v[18:33], v[166:169], v[202:205], v[18:33]
	s_waitcnt lgkmcnt(0)
	v_mfma_f32_32x32x16_f16 v[2:17], v[166:169], v[206:209], v[2:17]
	v_add_co_u32_e32 v166, vcc, s14, v210
	s_nop 1
	v_addc_co_u32_e32 v167, vcc, 0, v211, vcc
	global_store_dwordx4 v[210:211], v[98:101], off nt
	global_store_dwordx4 v[194:195], v[102:105], off nt
	global_store_dwordx4 v[196:197], v[106:109], off nt
	global_store_dwordx4 v[166:167], v[110:113], off nt
	v_mfma_f32_32x32x16_f16 v[82:97], v[162:165], v[142:145], v[82:97]
	s_barrier
	s_cbranch_scc1 .Ll2f_top
